# mLSTM gate scans in the state-increment items: DPP row shifts/broadcasts instead of 24 ds_bpermute round trips (on top of v20)
# speedup vs baseline: 1.0066x; 1.0016x over previous
.LBB0_583:
	s_or_b64 exec, exec, s[0:1]
	s_barrier
	v_mov_b32 v66, v0
	s_lshl_b32 s0, s35, 4
	v_ashrrev_i32_e32 v74, 6, v66
	s_lshl_b32 s1, s9, 1
	s_or_b32 s15, s1, s0
	v_cmp_gt_i32_e32 vcc, 2, v74
	s_and_saveexec_b64 s[30:31], vcc
	s_cbranch_execz .LBB0_589
	s_load_dwordx2 s[0:1], s[76:77], 0x138
	s_movk_i32 s37, 0x7f
	v_and_b32_e32 v68, 63, v66
	v_bitop3_b32 v67, v66, s37, 63 bitop3:0x6c
	v_cmp_gt_u32_e32 vcc, 64, v66
	v_bitop3_b32 v66, v66, 63, v66 bitop3:0xc
	v_lshlrev_b32_e32 v70, 4, v74
	v_cndmask_b32_e32 v73, v67, v68, vcc
	v_or_b32_e32 v67, 64, v68
	v_cndmask_b32_e32 v69, v66, v67, vcc
	v_or_b32_e32 v66, s36, v73
	v_lshlrev_b32_e32 v194, 7, v66
	v_ashrrev_i32_e32 v71, 31, v70
	s_waitcnt lgkmcnt(0)
	v_lshl_add_u64 v[66:67], s[0:1], 0, v[194:195]
	v_lshlrev_b64 v[70:71], 2, v[70:71]
	v_lshl_add_u64 v[66:67], v[66:67], 0, v[70:71]
	s_lshl_b32 s40, s9, 2
	s_mov_b32 s41, s71
	v_lshl_add_u64 v[76:77], v[66:67], 0, s[40:41]
	v_or_b32_e32 v66, s36, v69
	v_lshlrev_b32_e32 v194, 7, v66
	global_load_dword v72, v[76:77], off offset:32
	v_lshl_add_u64 v[66:67], s[0:1], 0, v[194:195]
	v_lshl_add_u64 v[66:67], v[66:67], 0, v[70:71]
	v_lshl_add_u64 v[66:67], v[66:67], 0, s[40:41]
	global_load_dword v70, v[66:67], off offset:32
	s_nop 0
	global_load_dword v67, v[66:67], off
	s_nop 0
	global_load_dword v66, v[76:77], off
	s_mov_b32 s0, 0xbfb8aa3b
	s_mov_b32 s36, 0x3f2aaaab
	s_mov_b32 s37, 0x3f317218
	s_mov_b32 s40, 0x7f800000
	s_mov_b32 s42, 0x33800000
	v_cmp_gt_u32_e64 s[44:45], 16, v68
	v_cmp_gt_u32_e64 s[46:47], 32, v68
	s_waitcnt vmcnt(3)
	v_max_f32_e32 v71, v72, v72
	v_mul_f32_e64 v72, |v72|, s0
	v_exp_f32_e32 v72, v72
	v_min_f32_e32 v75, 0, v71
	s_waitcnt vmcnt(2)
	v_max_f32_e32 v71, v70, v70
	v_mul_f32_e64 v70, |v70|, s0
	v_exp_f32_e32 v77, v70
	v_add_f32_e32 v78, 1.0, v72
	v_min_f32_e32 v76, 0, v71
	v_add_f32_e32 v79, -1.0, v78
	v_frexp_mant_f32_e32 v80, v78
	v_cvt_f64_f32_e32 v[70:71], v78
	v_add_f32_e32 v81, 1.0, v77
	v_sub_f32_e32 v82, v79, v78
	v_frexp_exp_i32_f64_e32 v83, v[70:71]
	v_cmp_gt_f32_e64 s[0:1], s36, v80
	v_sub_f32_e32 v79, v72, v79
	v_add_f32_e32 v84, -1.0, v81
	v_cvt_f64_f32_e32 v[70:71], v81
	v_add_f32_e32 v82, 1.0, v82
	v_subbrev_co_u32_e64 v80, s[0:1], 0, v83, s[0:1]
	v_sub_f32_e32 v83, v84, v81
	v_frexp_exp_i32_f64_e32 v70, v[70:71]
	v_add_f32_e32 v71, v79, v82
	v_sub_u32_e32 v79, 0, v80
	v_sub_f32_e32 v84, v77, v84
	v_cvt_f32_i32_e32 v80, v80
	v_add_f32_e32 v82, 1.0, v83
	v_ldexp_f32 v78, v78, v79
	v_ldexp_f32 v71, v71, v79
	v_add_f32_e32 v79, v84, v82
	v_add_f32_e32 v82, -1.0, v78
	v_add_f32_e32 v83, 1.0, v78
	v_add_f32_e32 v84, 1.0, v82
	v_add_f32_e32 v86, -1.0, v83
	v_sub_f32_e32 v84, v78, v84
	v_sub_f32_e32 v78, v78, v86
	v_mul_f32_e32 v86, 0x3f317218, v80
	v_add_f32_e32 v84, v71, v84
	v_add_f32_e32 v71, v71, v78
	v_fma_f32 v78, v80, s37, -v86
	v_add_f32_e32 v87, v82, v84
	v_add_f32_e32 v88, v83, v71
	v_fmac_f32_e32 v78, 0xb102e308, v80
	v_sub_f32_e32 v80, v87, v82
	v_sub_f32_e32 v82, v88, v83
	v_rcp_f32_e32 v83, v88
	v_add_f32_e32 v89, v86, v78
	v_sub_f32_e32 v71, v71, v82
	v_sub_f32_e32 v82, v89, v86
	v_sub_f32_e32 v78, v78, v82
	v_mul_f32_e32 v82, v87, v83
	v_sub_f32_e32 v80, v84, v80
	v_mul_f32_e32 v84, v88, v82
	v_fma_f32 v86, v82, v88, -v84
	v_fmac_f32_e32 v86, v82, v71
	v_add_f32_e32 v90, v84, v86
	v_sub_f32_e32 v91, v87, v90
	v_sub_f32_e32 v84, v90, v84
	v_sub_f32_e32 v87, v87, v91
	v_sub_f32_e32 v84, v84, v86
	v_sub_f32_e32 v86, v87, v90
	v_add_f32_e32 v80, v80, v86
	v_add_f32_e32 v80, v84, v80
	v_add_f32_e32 v84, v91, v80
	v_mul_f32_e32 v86, v83, v84
	v_sub_f32_e32 v87, v91, v84
	v_mul_f32_e32 v90, v88, v86
	v_add_f32_e32 v80, v80, v87
	v_add_f32_e32 v87, v82, v86
	v_fma_f32 v88, v86, v88, -v90
	v_sub_f32_e32 v82, v87, v82
	v_fmac_f32_e32 v88, v86, v71
	v_sub_f32_e32 v71, v86, v82
	v_add_f32_e32 v82, v90, v88
	v_sub_f32_e32 v86, v82, v90
	v_sub_f32_e32 v90, v84, v82
	v_sub_f32_e32 v84, v84, v90
	v_sub_f32_e32 v82, v84, v82
	v_sub_f32_e32 v86, v86, v88
	v_add_f32_e32 v80, v80, v82
	v_add_f32_e32 v80, v86, v80
	v_add_f32_e32 v80, v90, v80
	v_mul_f32_e32 v80, v83, v80
	v_add_f32_e32 v71, v71, v80
	v_add_f32_e32 v80, v87, v71
	v_mul_f32_e32 v82, v80, v80
	v_fmamk_f32 v86, v82, 0x3e9b6dac, v221
	v_sub_f32_e32 v83, v80, v87
	v_ldexp_f32 v84, v80, 1
	v_mul_f32_e32 v80, v80, v82
	v_fmaak_f32 v82, v82, v86, 0x3f2aaada
	v_mul_f32_e32 v80, v80, v82
	v_add_f32_e32 v82, v84, v80
	v_sub_f32_e32 v71, v71, v83
	v_sub_f32_e32 v83, v82, v84
	v_ldexp_f32 v71, v71, 1
	v_sub_f32_e32 v80, v80, v83
	v_add_f32_e32 v71, v71, v80
	v_add_f32_e32 v80, v82, v71
	v_sub_f32_e32 v82, v80, v82
	v_add_f32_e32 v83, v89, v80
	v_sub_f32_e32 v71, v71, v82
	v_sub_f32_e32 v82, v83, v89
	v_sub_f32_e32 v84, v83, v82
	v_sub_f32_e32 v80, v80, v82
	v_add_f32_e32 v82, v78, v71
	v_sub_f32_e32 v84, v89, v84
	v_sub_f32_e32 v86, v82, v78
	v_add_f32_e32 v80, v80, v84
	v_sub_f32_e32 v84, v82, v86
	v_sub_f32_e32 v71, v71, v86
	v_sub_f32_e32 v78, v78, v84
	v_add_f32_e32 v80, v82, v80
	v_add_f32_e32 v71, v71, v78
	v_add_f32_e32 v78, v83, v80
	v_sub_f32_e32 v82, v78, v83
	v_sub_f32_e32 v80, v80, v82
	v_add_f32_e32 v71, v71, v80
	v_add_f32_e32 v71, v78, v71
	v_cmp_neq_f32_e64 s[0:1], s40, v72
	v_frexp_mant_f32_e32 v85, v81
	s_nop 0
	v_cndmask_b32_e64 v71, v231, v71, s[0:1]
	v_cmp_ngt_f32_e64 s[0:1], -1.0, v72
	s_nop 1
	v_cndmask_b32_e64 v71, v232, v71, s[0:1]
	v_cmp_neq_f32_e64 s[0:1], -1.0, v72
	s_nop 1
	v_cndmask_b32_e64 v71, v233, v71, s[0:1]
	v_cmp_lt_f32_e64 s[0:1], |v72|, s42
	s_nop 1
	v_cndmask_b32_e64 v71, v71, v72, s[0:1]
	v_cmp_gt_f32_e64 s[0:1], s36, v85
	v_sub_f32_e32 v71, v75, v71
	s_nop 0
	v_subbrev_co_u32_e64 v70, s[0:1], 0, v70, s[0:1]
	v_sub_u32_e32 v72, 0, v70
	v_ldexp_f32 v75, v81, v72
	v_add_f32_e32 v78, -1.0, v75
	v_add_f32_e32 v81, 1.0, v75
	v_ldexp_f32 v72, v79, v72
	v_add_f32_e32 v79, 1.0, v78
	v_add_f32_e32 v82, -1.0, v81
	v_sub_f32_e32 v79, v75, v79
	v_sub_f32_e32 v75, v75, v82
	v_add_f32_e32 v79, v72, v79
	v_add_f32_e32 v72, v72, v75
	v_add_f32_e32 v75, v81, v72
	v_rcp_f32_e32 v82, v75
	v_add_f32_e32 v80, v78, v79
	v_sub_f32_e32 v78, v80, v78
	v_sub_f32_e32 v78, v79, v78
	v_sub_f32_e32 v79, v75, v81
	v_sub_f32_e32 v72, v72, v79
	v_mul_f32_e32 v79, v80, v82
	v_mul_f32_e32 v81, v75, v79
	v_fma_f32 v83, v79, v75, -v81
	v_fmac_f32_e32 v83, v79, v72
	v_add_f32_e32 v84, v81, v83
	v_sub_f32_e32 v85, v80, v84
	v_sub_f32_e32 v80, v80, v85
	v_sub_f32_e32 v81, v84, v81
	v_sub_f32_e32 v80, v80, v84
	v_add_f32_e32 v78, v78, v80
	v_sub_f32_e32 v80, v81, v83
	v_add_f32_e32 v78, v80, v78
	v_add_f32_e32 v80, v85, v78
	v_mul_f32_e32 v81, v82, v80
	v_mul_f32_e32 v83, v75, v81
	v_fma_f32 v75, v81, v75, -v83
	v_fmac_f32_e32 v75, v81, v72
	v_sub_f32_e32 v72, v85, v80
	v_add_f32_e32 v72, v78, v72
	v_add_f32_e32 v78, v83, v75
	v_sub_f32_e32 v84, v80, v78
	v_sub_f32_e32 v80, v80, v84
	v_sub_f32_e32 v83, v78, v83
	v_sub_f32_e32 v78, v80, v78
	v_add_f32_e32 v72, v72, v78
	v_sub_f32_e32 v75, v83, v75
	v_cvt_f32_i32_e32 v70, v70
	v_add_f32_e32 v72, v75, v72
	v_add_f32_e32 v75, v79, v81
	v_add_f32_e32 v72, v84, v72
	v_sub_f32_e32 v78, v75, v79
	v_mul_f32_e32 v72, v82, v72
	v_sub_f32_e32 v78, v81, v78
	v_add_f32_e32 v72, v78, v72
	v_mul_f32_e32 v81, 0x3f317218, v70
	v_add_f32_e32 v78, v75, v72
	v_fma_f32 v82, v70, s37, -v81
	v_mul_f32_e32 v79, v78, v78
	v_fmac_f32_e32 v82, 0xb102e308, v70
	v_sub_f32_e32 v70, v78, v75
	v_fmamk_f32 v80, v79, 0x3e9b6dac, v221
	v_sub_f32_e32 v70, v72, v70
	v_add_f32_e32 v72, v81, v82
	v_fmaak_f32 v80, v79, v80, 0x3f2aaada
	v_sub_f32_e32 v75, v72, v81
	v_ldexp_f32 v81, v78, 1
	v_mul_f32_e32 v78, v78, v79
	v_mul_f32_e32 v78, v78, v80
	v_add_f32_e32 v79, v81, v78
	v_sub_f32_e32 v80, v79, v81
	v_ldexp_f32 v70, v70, 1
	v_sub_f32_e32 v78, v78, v80
	v_add_f32_e32 v70, v70, v78
	v_add_f32_e32 v78, v79, v70
	v_sub_f32_e32 v79, v78, v79
	v_sub_f32_e32 v70, v70, v79
	v_add_f32_e32 v79, v72, v78
	v_sub_f32_e32 v80, v79, v72
	v_sub_f32_e32 v81, v79, v80
	v_sub_f32_e32 v75, v82, v75
	v_sub_f32_e32 v72, v72, v81
	v_sub_f32_e32 v78, v78, v80
	v_add_f32_e32 v72, v78, v72
	v_add_f32_e32 v78, v75, v70
	v_sub_f32_e32 v80, v78, v75
	v_sub_f32_e32 v81, v78, v80
	v_add_f32_e32 v72, v78, v72
	v_sub_f32_e32 v70, v70, v80
	v_sub_f32_e32 v75, v75, v81
	v_add_f32_e32 v70, v70, v75
	v_add_f32_e32 v75, v79, v72
	v_sub_f32_e32 v79, v75, v79
	v_sub_f32_e32 v72, v72, v79
	v_add_f32_e32 v70, v70, v72
	v_add_f32_e32 v70, v75, v70
	v_cmp_neq_f32_e64 s[36:37], s40, v77
	s_nop 1
	v_cndmask_b32_e64 v70, v231, v70, s[36:37]
	v_cmp_ngt_f32_e64 s[36:37], -1.0, v77
	v_cmp_neq_f32_e64 s[40:41], -1.0, v77
	s_nop 1
	v_cndmask_b32_e64 v70, v232, v70, s[36:37]
	v_cndmask_b32_e64 v70, v233, v70, s[40:41]
	v_cmp_lt_f32_e64 s[40:41], |v77|, s42
	s_nop 1
	v_cndmask_b32_e64 v70, v70, v77, s[40:41]
	v_sub_f32_e32 v70, v76, v70
	s_nop 1
	v_add_f32_dpp v71, v71, v71 row_shr:1 row_mask:0xf bank_mask:0xf
	v_add_f32_dpp v70, v70, v70 row_shr:1 row_mask:0xf bank_mask:0xf
	s_nop 1
	v_add_f32_dpp v71, v71, v71 row_shr:2 row_mask:0xf bank_mask:0xf
	v_add_f32_dpp v70, v70, v70 row_shr:2 row_mask:0xf bank_mask:0xf
	s_nop 1
	v_add_f32_dpp v71, v71, v71 row_shr:4 row_mask:0xf bank_mask:0xf
	v_add_f32_dpp v70, v70, v70 row_shr:4 row_mask:0xf bank_mask:0xf
	s_nop 1
	v_add_f32_dpp v71, v71, v71 row_shr:8 row_mask:0xf bank_mask:0xf
	v_add_f32_dpp v70, v70, v70 row_shr:8 row_mask:0xf bank_mask:0xf
	s_nop 1
	v_add_f32_dpp v71, v71, v71 row_bcast:15 row_mask:0xa bank_mask:0xf
	v_add_f32_dpp v70, v70, v70 row_bcast:15 row_mask:0xa bank_mask:0xf
	s_nop 1
	v_add_f32_dpp v71, v71, v71 row_bcast:31 row_mask:0xc bank_mask:0xf
	v_add_f32_dpp v70, v70, v70 row_bcast:31 row_mask:0xc bank_mask:0xf
	s_nop 1
	v_readlane_b32 s58, v71, 63
	s_waitcnt vmcnt(0)
	v_mov_b32_e32 v75, v70
	v_mov_b32_e32 v70, v71
	v_add_f32_e32 v75, s58, v75
	v_sub_f32_e32 v71, v66, v70
	v_sub_f32_e32 v67, v67, v75
	v_mov_b32_e32 v66, v75
	v_mov_b32_e32 v72, v71
	v_mov_b32_e32 v76, v67
	s_nop 1
	v_max_f32_dpp v72, v72, v72 row_shr:1 row_mask:0xf bank_mask:0xf
	v_max_f32_dpp v76, v76, v76 row_shr:1 row_mask:0xf bank_mask:0xf
	s_nop 1
	v_max_f32_dpp v72, v72, v72 row_shr:2 row_mask:0xf bank_mask:0xf
	v_max_f32_dpp v76, v76, v76 row_shr:2 row_mask:0xf bank_mask:0xf
	s_nop 1
	v_max_f32_dpp v72, v72, v72 row_shr:4 row_mask:0xf bank_mask:0xf
	v_max_f32_dpp v76, v76, v76 row_shr:4 row_mask:0xf bank_mask:0xf
	s_nop 1
	v_max_f32_dpp v72, v72, v72 row_shr:8 row_mask:0xf bank_mask:0xf
	v_max_f32_dpp v76, v76, v76 row_shr:8 row_mask:0xf bank_mask:0xf
	s_nop 1
	v_max_f32_dpp v72, v72, v72 row_bcast:15 row_mask:0xa bank_mask:0xf
	v_max_f32_dpp v76, v76, v76 row_bcast:15 row_mask:0xa bank_mask:0xf
	s_nop 1
	v_max_f32_dpp v72, v72, v72 row_bcast:31 row_mask:0xc bank_mask:0xf
	v_max_f32_dpp v76, v76, v76 row_bcast:31 row_mask:0xc bank_mask:0xf
	s_nop 1
	v_readlane_b32 s37, v72, 63
	v_cmp_ne_u32_e64 s[0:1], 0, v68
	s_nop 1
	v_max_f32_e32 v68, s37, v76
	s_nop 1
	v_lshl_add_u32 v76, v74, 9, 0
	v_readlane_b32 s37, v68, 63
	v_lshl_add_u32 v78, v73, 2, v76
	v_readlane_b32 s36, v66, 63
	v_subrev_f32_e32 v75, s37, v71
	v_mul_f32_e32 v75, 0x3fb8aa3b, v75
	v_subrev_f32_e32 v77, s37, v67
	v_exp_f32_e32 v75, v75
	v_mul_f32_e32 v77, 0x3fb8aa3b, v77
	v_exp_f32_e32 v77, v77
	ds_write_b32 v78, v75 offset:52288
	v_lshl_add_u32 v75, v69, 2, v76
	v_add_u32_e32 v76, s15, v74
	ds_write_b32 v75, v77 offset:52288
	s_and_saveexec_b64 s[40:41], s[0:1]
	s_xor_b64 s[0:1], exec, s[40:41]
	s_and_b64 s[40:41], s[56:57], exec
	s_cselect_b32 s40, 0x41, 1
	s_sub_i32 s40, s40, s34
	v_mov_b32_e32 v74, s40
	v_mov_b32_e32 v75, s14
	v_cndmask_b32_e32 v74, v74, v75, vcc
	v_ashrrev_i32_e32 v75, 31, v74
	s_movk_i32 s40, 0x42
	v_mad_i64_i32 v[74:75], s[40:41], v76, s40, v[74:75]
	s_andn2_saveexec_b64 s[0:1], s[0:1]
	s_cbranch_execz .LBB0_588
	s_and_b64 s[42:43], s[56:57], exec
	s_cselect_b32 s42, 0x41, 1
	s_load_dwordx2 s[40:41], s[76:77], 0x190
	s_sub_i32 s42, s42, s34
	v_mov_b32_e32 v74, s42
	v_mov_b32_e32 v75, s14
	v_cndmask_b32_e32 v74, v74, v75, vcc
	v_ashrrev_i32_e32 v75, 31, v74
	s_movk_i32 s42, 0x42
	v_mad_i64_i32 v[74:75], s[42:43], v76, s42, v[74:75]
	v_mov_b32_e32 v78, s37
	s_waitcnt lgkmcnt(0)
	v_lshl_add_u64 v[76:77], v[74:75], 3, s[40:41]
	v_add_f32_e32 v79, s36, v78
	v_mov_b32_e32 v78, s36
	global_store_dwordx2 v[76:77], v[78:79], off
